# v18: lever 7 - the 127 packed fp32 ops (v_pk_mul/fma/add_f32) of the scan helper loop split into scalar ops
# speedup vs baseline: 1.0018x; 1.0018x over previous
.LBB0_1764:
	ds_read_b64_tr_b16 v[48:49], v221
	ds_read_b64_tr_b16 v[58:59], v222
	ds_read_b64_tr_b16 v[60:61], v223
	ds_read_b64_tr_b16 v[50:51], v224
	ds_read_b64_tr_b16 v[52:53], v225
	ds_read_b64_tr_b16 v[66:67], v226
	ds_read_b64_tr_b16 v[68:69], v227
	ds_read_b64_tr_b16 v[62:63], v228
	ds_read_b64_tr_b16 v[64:65], v229
	ds_read_b64_tr_b16 v[54:55], v230
	ds_read_b64_tr_b16 v[56:57], v231
	ds_read_b64_tr_b16 v[70:71], v232
	ds_read_b64_tr_b16 v[80:81], v233
	ds_read_b64_tr_b16 v[44:45], v234
	ds_read_b64_tr_b16 v[46:47], v235
	ds_read_b64_tr_b16 v[82:83], v236
	s_waitcnt lgkmcnt(0)
	s_lshl_b32 s0, s56, 13
	s_add_i32 s73, s77, s0
	v_lshlrev_b32_e32 v84, 16, v48
	v_lshlrev_b32_e32 v98, 16, v63
	v_and_b32_e32 v99, 0xffff0000, v63
	v_add_f32_e32 v63, 0, v84
	v_and_b32_e32 v85, 0xffff0000, v48
	v_lshlrev_b32_e32 v88, 16, v50
	v_and_b32_e32 v89, 0xffff0000, v50
	v_lshlrev_b32_e32 v90, 16, v51
	v_and_b32_e32 v91, 0xffff0000, v51
	v_readlane_b32 s30, v75, 0
	v_mul_f32_e32 v48, 0x3fb8aa3b, v63
	v_lshlrev_b32_e32 v50, 16, v58
	v_lshlrev_b32_e32 v51, 16, v60
	v_lshlrev_b32_e32 v92, 16, v52
	v_and_b32_e32 v93, 0xffff0000, v52
	v_lshlrev_b32_e32 v94, 16, v53
	v_and_b32_e32 v95, 0xffff0000, v53
	v_lshlrev_b32_e32 v96, 16, v62
	v_and_b32_e32 v97, 0xffff0000, v62
	v_lshlrev_b32_e32 v100, 16, v64
	v_and_b32_e32 v101, 0xffff0000, v64
	v_lshlrev_b32_e32 v102, 16, v65
	v_and_b32_e32 v103, 0xffff0000, v65
	v_lshlrev_b32_e32 v104, 16, v70
	v_and_b32_e32 v105, 0xffff0000, v70
	v_exp_f32_e64 v62, -v48
	v_exp_f32_e32 v48, v48
	v_add_f32_e32 v53, -1.0, v50
	v_mov_b32_e32 v52, s30
	v_mul_f32_e32 v64, s30, v42
	v_mul_f32_e32 v65, s31, v43
	v_mov_b32_e32 v70, v51
	v_mul_f32_e32 v64, v64, v70
	v_mul_f32_e32 v65, v65, v71
	v_fma_f32 v52, v42, v52, s2
	v_fma_f32 v53, v43, v53, s3
	v_lshlrev_b32_e32 v86, 16, v49
	v_mov_b32_e32 v65, v53
	v_mul_f32_e32 v50, v64, v50
	v_mul_f32_e32 v51, v65, v51
	v_and_b32_e32 v87, 0xffff0000, v49
	v_mul_f32_e32 v49, v48, v51
	v_mul_f32_e32 v48, v48, v50
	v_mul_f32_e32 v52, v62, v88
	v_mul_f32_e32 v50, -1.0, v64
	v_mul_f32_e32 v51, -1.0, v65
	v_lshlrev_b32_e32 v111, 16, v82
	v_and_b32_e32 v112, 0xffff0000, v82
	v_readlane_b32 s0, v75, 1
	v_readlane_b32 s96, v75, 2
	v_readlane_b32 s94, v75, 3
	v_readlane_b32 s92, v75, 4
	v_readlane_b32 s90, v75, 5
	v_readlane_b32 s88, v75, 6
	v_readlane_b32 s86, v75, 7
	v_readlane_b32 s84, v75, 8
	v_readlane_b32 s82, v75, 9
	v_readlane_b32 s80, v75, 10
	v_readlane_b32 s78, v75, 11
	v_readlane_b32 s76, v75, 12
	v_readlane_b32 s74, v75, 13
	v_readlane_b32 s72, v75, 14
	v_readlane_b32 s56, v75, 15
	v_add_u32_e32 v75, s89, v237
	v_cvt_pk_bf16_f32 v50, v50, v52
	v_add_f32_e32 v82, v63, v85
	v_cvt_pk_bf16_f32 v51, v48, v49
	ds_write_b16 v75, v50
	ds_write_b16_d16_hi v75, v50 offset:2304
	ds_write_b16 v74, v51
	ds_write_b16_d16_hi v74, v51 offset:2304
	v_mul_f32_e32 v50, 0x3fb8aa3b, v82
	v_and_b32_e32 v52, 0xffff0000, v58
	v_lshlrev_b32_e32 v106, 16, v71
	v_and_b32_e32 v107, 0xffff0000, v71
	v_exp_f32_e64 v63, -v50
	v_exp_f32_e32 v50, v50
	v_and_b32_e32 v53, 0xffff0000, v60
	v_add_f32_e32 v65, -1.0, v52
	v_mov_b32_e32 v64, s0
	v_mul_f32_e32 v70, s0, v42
	v_mul_f32_e32 v71, s1, v43
	v_fma_f32 v64, v42, v64, s2
	v_fma_f32 v65, v43, v65, s3
	v_mul_f32_e32 v70, v70, v53
	v_mul_f32_e32 v71, v71, v52
	v_add_f32_e32 v60, v82, v86
	v_mov_b32_e32 v71, v65
	v_mul_f32_e32 v52, v70, v52
	v_mul_f32_e32 v53, v71, v53
	v_lshlrev_b32_e32 v108, 16, v80
	v_mul_f32_e32 v51, v50, v53
	v_mul_f32_e32 v50, v50, v52
	v_mul_f32_e32 v52, -1.0, v70
	v_mul_f32_e32 v53, -1.0, v71
	v_lshlrev_b32_e32 v70, 16, v59
	v_mov_b32_e32 v53, v89
	v_mul_f32_e32 v52, v62, v52
	v_mul_f32_e32 v53, v63, v53
	v_lshlrev_b32_e32 v71, 16, v61
	v_cvt_pk_bf16_f32 v52, v52, v53
	v_and_b32_e32 v109, 0xffff0000, v80
	v_lshlrev_b32_e32 v110, 16, v81
	v_and_b32_e32 v80, 0xffff0000, v81
	v_lshlrev_b32_e32 v81, 16, v83
	v_and_b32_e32 v79, 0xffff0000, v83
	v_cvt_pk_bf16_f32 v53, v50, v51
	ds_write_b16 v75, v52 offset:144
	ds_write_b16_d16_hi v75, v52 offset:2448
	ds_write_b16 v74, v53 offset:144
	ds_write_b16_d16_hi v74, v53 offset:2448
	v_mul_f32_e32 v52, 0x3fb8aa3b, v60
	v_add_f32_e32 v83, -1.0, v70
	v_mov_b32_e32 v82, s96
	v_mul_f32_e32 v84, s96, v42
	v_mul_f32_e32 v85, s97, v43
	v_mov_b32_e32 v58, v71
	v_exp_f32_e64 v65, -v52
	v_mul_f32_e32 v84, v84, v58
	v_mul_f32_e32 v85, v85, v59
	v_fma_f32 v82, v42, v82, s2
	v_fma_f32 v83, v43, v83, s3
	v_exp_f32_e32 v52, v52
	v_mov_b32_e32 v85, v83
	v_mov_b32_e32 v64, v63
	v_mul_f32_e32 v62, -1.0, v84
	v_mul_f32_e32 v63, -1.0, v85
	v_mul_f32_e32 v70, v84, v70
	v_mul_f32_e32 v71, v85, v71
	v_mov_b32_e32 v63, v90
	v_mul_f32_e32 v62, v64, v62
	v_mul_f32_e32 v63, v65, v63
	v_mul_f32_e32 v53, v52, v71
	v_mul_f32_e32 v52, v52, v70
	v_cvt_pk_bf16_f32 v58, v62, v63
	v_add_f32_e32 v64, v60, v87
	v_cvt_pk_bf16_f32 v62, v52, v53
	ds_write_b16 v75, v58 offset:288
	ds_write_b16_d16_hi v75, v58 offset:2592
	ds_write_b16 v74, v62 offset:288
	ds_write_b16_d16_hi v74, v62 offset:2592
	v_mul_f32_e32 v58, 0x3fb8aa3b, v64
	v_and_b32_e32 v60, 0xffff0000, v59
	v_exp_f32_e64 v63, -v58
	v_exp_f32_e32 v58, v58
	v_and_b32_e32 v61, 0xffff0000, v61
	v_add_f32_e32 v71, -1.0, v60
	v_mov_b32_e32 v70, s94
	v_mul_f32_e32 v82, s94, v42
	v_mul_f32_e32 v83, s95, v43
	v_fma_f32 v70, v42, v70, s2
	v_fma_f32 v71, v43, v71, s3
	v_mul_f32_e32 v82, v82, v61
	v_mul_f32_e32 v83, v83, v60
	v_mov_b32_e32 v62, v65
	v_mov_b32_e32 v83, v71
	v_mul_f32_e32 v60, v82, v60
	v_mul_f32_e32 v61, v83, v61
	v_add_f32_e32 v86, v64, v92
	v_mul_f32_e32 v59, v58, v61
	v_mul_f32_e32 v58, v58, v60
	v_mul_f32_e32 v60, -1.0, v82
	v_mul_f32_e32 v61, -1.0, v83
	v_lshlrev_b32_e32 v70, 16, v66
	v_mov_b32_e32 v61, v91
	v_mul_f32_e32 v60, v62, v60
	v_mul_f32_e32 v61, v63, v61
	v_lshlrev_b32_e32 v71, 16, v68
	v_cvt_pk_bf16_f32 v60, v60, v61
	v_cvt_pk_bf16_f32 v61, v58, v59
	ds_write_b16 v75, v60 offset:432
	ds_write_b16_d16_hi v75, v60 offset:2736
	ds_write_b16 v74, v61 offset:432
	ds_write_b16_d16_hi v74, v61 offset:2736
	v_mul_f32_e32 v60, 0x3fb8aa3b, v86
	v_add_f32_e32 v83, -1.0, v70
	v_mov_b32_e32 v82, s92
	v_mul_f32_e32 v84, s92, v42
	v_mul_f32_e32 v85, s93, v43
	v_mov_b32_e32 v62, v71
	v_exp_f32_e64 v65, -v60
	v_mul_f32_e32 v84, v84, v62
	v_mul_f32_e32 v85, v85, v63
	v_fma_f32 v82, v42, v82, s2
	v_fma_f32 v83, v43, v83, s3
	v_exp_f32_e32 v60, v60
	v_mov_b32_e32 v85, v83
	v_mov_b32_e32 v64, v63
	v_mul_f32_e32 v62, -1.0, v84
	v_mul_f32_e32 v63, -1.0, v85
	v_mul_f32_e32 v70, v84, v70
	v_mul_f32_e32 v71, v85, v71
	v_mov_b32_e32 v63, v96
	v_mul_f32_e32 v62, v64, v62
	v_mul_f32_e32 v63, v65, v63
	v_mul_f32_e32 v61, v60, v71
	v_mul_f32_e32 v60, v60, v70
	v_cvt_pk_bf16_f32 v62, v62, v63
	v_add_f32_e32 v88, v86, v93
	v_and_b32_e32 v82, 0xffff0000, v66
	v_cvt_pk_bf16_f32 v63, v60, v61
	ds_write_b16 v75, v62 offset:576
	ds_write_b16_d16_hi v75, v62 offset:2880
	ds_write_b16 v74, v63 offset:576
	ds_write_b16_d16_hi v74, v63 offset:2880
	v_mul_f32_e32 v62, 0x3fb8aa3b, v88
	v_and_b32_e32 v83, 0xffff0000, v68
	v_add_f32_e32 v85, -1.0, v82
	v_mov_b32_e32 v84, s90
	v_mul_f32_e32 v86, s90, v42
	v_mul_f32_e32 v87, s91, v43
	v_exp_f32_e64 v71, -v62
	v_mul_f32_e32 v86, v86, v83
	v_mul_f32_e32 v87, v87, v82
	v_fma_f32 v84, v42, v84, s2
	v_fma_f32 v85, v43, v85, s3
	v_exp_f32_e32 v62, v62
	v_mov_b32_e32 v87, v85
	v_mov_b32_e32 v70, v65
	v_mul_f32_e32 v64, -1.0, v86
	v_mul_f32_e32 v65, -1.0, v87
	v_mul_f32_e32 v82, v86, v82
	v_mul_f32_e32 v83, v87, v83
	v_mov_b32_e32 v65, v97
	v_mul_f32_e32 v64, v70, v64
	v_mul_f32_e32 v65, v71, v65
	v_mul_f32_e32 v63, v62, v83
	v_mul_f32_e32 v62, v62, v82
	v_cvt_pk_bf16_f32 v64, v64, v65
	v_add_f32_e32 v68, v88, v94
	v_lshlrev_b32_e32 v84, 16, v67
	v_lshlrev_b32_e32 v85, 16, v69
	v_cvt_pk_bf16_f32 v65, v62, v63
	ds_write_b16 v75, v64 offset:720
	ds_write_b16_d16_hi v75, v64 offset:3024
	ds_write_b16 v74, v65 offset:720
	ds_write_b16_d16_hi v74, v65 offset:3024
	v_mul_f32_e32 v64, 0x3fb8aa3b, v68
	v_add_f32_e32 v87, -1.0, v84
	v_mov_b32_e32 v86, s88
	v_mul_f32_e32 v88, s88, v42
	v_mul_f32_e32 v89, s89, v43
	v_mov_b32_e32 v66, v85
	v_exp_f32_e64 v83, -v64
	v_mul_f32_e32 v88, v88, v66
	v_mul_f32_e32 v89, v89, v67
	v_fma_f32 v86, v42, v86, s2
	v_fma_f32 v87, v43, v87, s3
	v_exp_f32_e32 v64, v64
	v_mov_b32_e32 v89, v87
	v_mov_b32_e32 v82, v71
	v_mul_f32_e32 v70, -1.0, v88
	v_mul_f32_e32 v71, -1.0, v89
	v_mul_f32_e32 v84, v88, v84
	v_mul_f32_e32 v85, v89, v85
	v_mov_b32_e32 v71, v98
	v_mul_f32_e32 v70, v82, v70
	v_mul_f32_e32 v71, v83, v71
	v_mul_f32_e32 v65, v64, v85
	v_mul_f32_e32 v64, v64, v84
	v_cvt_pk_bf16_f32 v66, v70, v71
	v_add_f32_e32 v82, v68, v95
	v_cvt_pk_bf16_f32 v70, v64, v65
	ds_write_b16 v75, v66 offset:864
	ds_write_b16_d16_hi v75, v66 offset:3168
	ds_write_b16 v74, v70 offset:864
	ds_write_b16_d16_hi v74, v70 offset:3168
	v_mul_f32_e32 v66, 0x3fb8aa3b, v82
	v_and_b32_e32 v68, 0xffff0000, v67
	v_exp_f32_e64 v71, -v66
	v_exp_f32_e32 v66, v66
	v_and_b32_e32 v69, 0xffff0000, v69
	v_add_f32_e32 v85, -1.0, v68
	v_mov_b32_e32 v84, s86
	v_mul_f32_e32 v86, s86, v42
	v_mul_f32_e32 v87, s87, v43
	v_fma_f32 v84, v42, v84, s2
	v_fma_f32 v85, v43, v85, s3
	v_mul_f32_e32 v86, v86, v69
	v_mul_f32_e32 v87, v87, v68
	v_mov_b32_e32 v70, v83
	v_mov_b32_e32 v87, v85
	v_mul_f32_e32 v68, v86, v68
	v_mul_f32_e32 v69, v87, v69
	v_add_f32_e32 v90, v82, v100
	v_mul_f32_e32 v67, v66, v69
	v_mul_f32_e32 v66, v66, v68
	v_mul_f32_e32 v68, -1.0, v86
	v_mul_f32_e32 v69, -1.0, v87
	v_lshlrev_b32_e32 v84, 16, v54
	v_mov_b32_e32 v69, v99
	v_mul_f32_e32 v68, v70, v68
	v_mul_f32_e32 v69, v71, v69
	v_lshlrev_b32_e32 v85, 16, v56
	v_cvt_pk_bf16_f32 v68, v68, v69
	v_cvt_pk_bf16_f32 v69, v66, v67
	ds_write_b16 v75, v68 offset:1008
	ds_write_b16_d16_hi v75, v68 offset:3312
	ds_write_b16 v74, v69 offset:1008
	ds_write_b16_d16_hi v74, v69 offset:3312
	v_mul_f32_e32 v68, 0x3fb8aa3b, v90
	v_add_f32_e32 v87, -1.0, v84
	v_mov_b32_e32 v86, s84
	v_mul_f32_e32 v88, s84, v42
	v_mul_f32_e32 v89, s85, v43
	v_mov_b32_e32 v70, v85
	v_exp_f32_e64 v83, -v68
	v_mul_f32_e32 v88, v88, v70
	v_mul_f32_e32 v89, v89, v71
	v_fma_f32 v86, v42, v86, s2
	v_fma_f32 v87, v43, v87, s3
	v_exp_f32_e32 v68, v68
	v_mov_b32_e32 v89, v87
	v_mov_b32_e32 v82, v71
	v_mul_f32_e32 v70, -1.0, v88
	v_mul_f32_e32 v71, -1.0, v89
	v_mul_f32_e32 v84, v88, v84
	v_mul_f32_e32 v85, v89, v85
	v_mov_b32_e32 v71, v104
	v_mul_f32_e32 v70, v82, v70
	v_mul_f32_e32 v71, v83, v71
	v_mul_f32_e32 v69, v68, v85
	v_mul_f32_e32 v68, v68, v84
	v_cvt_pk_bf16_f32 v70, v70, v71
	v_add_f32_e32 v92, v90, v101
	v_and_b32_e32 v86, 0xffff0000, v54
	v_cvt_pk_bf16_f32 v71, v68, v69
	ds_write_b16 v75, v70 offset:1152
	ds_write_b16_d16_hi v75, v70 offset:3456
	ds_write_b16 v74, v71 offset:1152
	ds_write_b16_d16_hi v74, v71 offset:3456
	v_mul_f32_e32 v70, 0x3fb8aa3b, v92
	v_and_b32_e32 v87, 0xffff0000, v56
	v_add_f32_e32 v89, -1.0, v86
	v_mov_b32_e32 v88, s82
	v_mul_f32_e32 v90, s82, v42
	v_mul_f32_e32 v91, s83, v43
	v_exp_f32_e64 v85, -v70
	v_exp_f32_e32 v70, v70
	v_mul_f32_e32 v90, v90, v87
	v_mul_f32_e32 v91, v91, v86
	v_fma_f32 v88, v42, v88, s2
	v_fma_f32 v89, v43, v89, s3
	v_mov_b32_e32 v84, v83
	v_mov_b32_e32 v91, v89
	v_mul_f32_e32 v82, -1.0, v90
	v_mul_f32_e32 v83, -1.0, v91
	v_mul_f32_e32 v86, v90, v86
	v_mul_f32_e32 v87, v91, v87
	v_mov_b32_e32 v83, v105
	v_mul_f32_e32 v71, v70, v87
	v_mul_f32_e32 v70, v70, v86
	v_mul_f32_e32 v82, v84, v82
	v_mul_f32_e32 v83, v85, v83
	v_cvt_pk_bf16_f32 v56, v70, v71
	v_cvt_pk_bf16_f32 v54, v82, v83
	v_add_f32_e32 v92, v92, v102
	v_lshlrev_b32_e32 v86, 16, v55
	v_lshlrev_b32_e32 v87, 16, v57
	ds_write_b16 v75, v54 offset:1296
	ds_write_b16_d16_hi v75, v54 offset:3600
	ds_write_b16 v74, v56 offset:1296
	ds_write_b16_d16_hi v74, v56 offset:3600
	v_mul_f32_e32 v54, 0x3fb8aa3b, v92
	v_add_f32_e32 v89, -1.0, v86
	v_mov_b32_e32 v88, s80
	v_mul_f32_e32 v90, s80, v42
	v_mul_f32_e32 v91, s81, v43
	v_mov_b32_e32 v56, v87
	v_exp_f32_e64 v83, -v54
	v_exp_f32_e32 v54, v54
	v_mul_f32_e32 v90, v90, v56
	v_mul_f32_e32 v91, v91, v57
	v_fma_f32 v88, v42, v88, s2
	v_fma_f32 v89, v43, v89, s3
	v_mov_b32_e32 v82, v85
	v_mov_b32_e32 v91, v89
	v_mul_f32_e32 v84, -1.0, v90
	v_mul_f32_e32 v85, -1.0, v91
	v_mul_f32_e32 v86, v90, v86
	v_mul_f32_e32 v87, v91, v87
	v_mov_b32_e32 v85, v106
	v_mul_f32_e32 v86, v54, v86
	v_mul_f32_e32 v87, v54, v87
	v_mul_f32_e32 v84, v82, v84
	v_mul_f32_e32 v85, v83, v85
	v_cvt_pk_bf16_f32 v56, v86, v87
	v_cvt_pk_bf16_f32 v54, v84, v85
	v_add_f32_e32 v82, v92, v103
	ds_write_b16 v75, v54 offset:1440
	ds_write_b16_d16_hi v75, v54 offset:3744
	ds_write_b16 v74, v56 offset:1440
	ds_write_b16_d16_hi v74, v56 offset:3744
	v_mul_f32_e32 v54, 0x3fb8aa3b, v82
	v_and_b32_e32 v56, 0xffff0000, v55
	v_exp_f32_e64 v85, -v54
	v_exp_f32_e32 v54, v54
	v_and_b32_e32 v57, 0xffff0000, v57
	v_add_f32_e32 v89, -1.0, v56
	v_mov_b32_e32 v88, s78
	v_mul_f32_e32 v90, s78, v42
	v_mul_f32_e32 v91, s79, v43
	v_fma_f32 v88, v42, v88, s2
	v_fma_f32 v89, v43, v89, s3
	v_mul_f32_e32 v90, v90, v57
	v_mul_f32_e32 v91, v91, v56
	v_mov_b32_e32 v84, v83
	v_mov_b32_e32 v91, v89
	v_mul_f32_e32 v56, v90, v56
	v_mul_f32_e32 v57, v91, v57
	v_add_f32_e32 v92, v82, v108
	v_mul_f32_e32 v55, v54, v57
	v_mul_f32_e32 v54, v54, v56
	v_mul_f32_e32 v56, -1.0, v90
	v_mul_f32_e32 v57, -1.0, v91
	v_lshlrev_b32_e32 v82, 16, v44
	v_mov_b32_e32 v57, v107
	v_mul_f32_e32 v56, v84, v56
	v_mul_f32_e32 v57, v85, v57
	v_lshlrev_b32_e32 v83, 16, v46
	v_cvt_pk_bf16_f32 v56, v56, v57
	v_cvt_pk_bf16_f32 v57, v54, v55
	ds_write_b16 v75, v56 offset:1584
	ds_write_b16_d16_hi v75, v56 offset:3888
	ds_write_b16 v74, v57 offset:1584
	ds_write_b16_d16_hi v74, v57 offset:3888
	v_mul_f32_e32 v56, 0x3fb8aa3b, v92
	v_exp_f32_e64 v57, -v56
	v_exp_f32_e32 v56, v56
	v_add_f32_e32 v89, -1.0, v82
	v_mov_b32_e32 v88, s76
	v_mul_f32_e32 v90, s76, v42
	v_mul_f32_e32 v91, s77, v43
	v_mov_b32_e32 v84, v83
	v_mul_f32_e32 v90, v90, v84
	v_mul_f32_e32 v91, v91, v85
	v_fma_f32 v88, v42, v88, s2
	v_fma_f32 v89, v43, v89, s3
	v_add_f32_e32 v94, v92, v109
	v_mov_b32_e32 v91, v89
	v_mul_f32_e32 v82, v90, v82
	v_mul_f32_e32 v83, v91, v83
	v_and_b32_e32 v88, 0xffff0000, v44
	v_mul_f32_e32 v82, v56, v82
	v_mul_f32_e32 v83, v56, v83
	v_mov_b32_e32 v56, v85
	v_mul_f32_e32 v84, -1.0, v90
	v_mul_f32_e32 v85, -1.0, v91
	v_and_b32_e32 v89, 0xffff0000, v46
	v_mov_b32_e32 v85, v111
	v_mul_f32_e32 v84, v56, v84
	v_mul_f32_e32 v85, v57, v85
	v_add_f32_e32 v91, -1.0, v88
	v_cvt_pk_bf16_f32 v56, v84, v85
	v_cvt_pk_bf16_f32 v84, v82, v83
	ds_write_b16 v75, v56 offset:1728
	ds_write_b16_d16_hi v75, v56 offset:4032
	ds_write_b16 v74, v84 offset:1728
	ds_write_b16_d16_hi v74, v84 offset:4032
	v_mul_f32_e32 v56, 0x3fb8aa3b, v94
	v_exp_f32_e64 v85, -v56
	v_exp_f32_e32 v56, v56
	v_mov_b32_e32 v90, s74
	v_mul_f32_e32 v92, s74, v42
	v_mul_f32_e32 v93, s75, v43
	v_fma_f32 v90, v42, v90, s2
	v_fma_f32 v91, v43, v91, s3
	v_mul_f32_e32 v92, v92, v89
	v_mul_f32_e32 v93, v93, v88
	v_mov_b32_e32 v84, v57
	v_mov_b32_e32 v93, v91
	v_mul_f32_e32 v88, v92, v88
	v_mul_f32_e32 v89, v93, v89
	v_add_f32_e32 v96, v94, v110
	v_mul_f32_e32 v88, v56, v88
	v_mul_f32_e32 v89, v56, v89
	v_mul_f32_e32 v56, -1.0, v92
	v_mul_f32_e32 v57, -1.0, v93
	v_cvt_pk_bf16_f32 v46, v88, v89
	v_mov_b32_e32 v57, v112
	v_mul_f32_e32 v56, v84, v56
	v_mul_f32_e32 v57, v85, v57
	v_lshlrev_b32_e32 v90, 16, v45
	v_cvt_pk_bf16_f32 v44, v56, v57
	v_lshlrev_b32_e32 v91, 16, v47
	ds_write_b16 v75, v44 offset:1872
	ds_write_b16_d16_hi v75, v44 offset:4176
	ds_write_b16 v74, v46 offset:1872
	ds_write_b16_d16_hi v74, v46 offset:4176
	v_mul_f32_e32 v44, 0x3fb8aa3b, v96
	v_add_f32_e32 v93, -1.0, v90
	v_mov_b32_e32 v92, s72
	v_mul_f32_e32 v94, s72, v42
	v_mul_f32_e32 v95, s73, v43
	v_mov_b32_e32 v46, v91
	v_exp_f32_e64 v57, -v44
	v_mul_f32_e32 v94, v94, v46
	v_mul_f32_e32 v95, v95, v47
	v_fma_f32 v92, v42, v92, s2
	v_fma_f32 v93, v43, v93, s3
	v_exp_f32_e32 v44, v44
	v_mov_b32_e32 v95, v93
	v_mov_b32_e32 v56, v85
	v_mul_f32_e32 v84, -1.0, v94
	v_mul_f32_e32 v85, -1.0, v95
	v_mul_f32_e32 v90, v94, v90
	v_mul_f32_e32 v91, v95, v91
	v_mov_b32_e32 v85, v81
	v_mul_f32_e32 v84, v56, v84
	v_mul_f32_e32 v85, v57, v85
	v_mul_f32_e32 v90, v44, v90
	v_mul_f32_e32 v91, v44, v91
	v_cvt_pk_bf16_f32 v44, v84, v85
	v_cvt_pk_bf16_f32 v46, v90, v91
	ds_write_b16 v75, v44 offset:2016
	ds_write_b16_d16_hi v75, v44 offset:4320
	ds_write_b16 v74, v46 offset:2016
	ds_write_b16_d16_hi v74, v46 offset:4320
	v_add_f32_e32 v44, v96, v80
	v_mul_f32_e32 v44, 0x3fb8aa3b, v44
	v_and_b32_e32 v46, 0xffff0000, v45
	v_exp_f32_e64 v81, -v44
	v_exp_f32_e32 v44, v44
	v_and_b32_e32 v47, 0xffff0000, v47
	v_add_f32_e32 v85, -1.0, v46
	v_mov_b32_e32 v84, s56
	v_mul_f32_e32 v92, s56, v42
	v_mul_f32_e32 v93, s57, v43
	v_fma_f32 v84, v42, v84, s2
	v_fma_f32 v85, v43, v85, s3
	v_mul_f32_e32 v92, v92, v47
	v_mul_f32_e32 v93, v93, v46
	v_mov_b32_e32 v80, v57
	v_mov_b32_e32 v93, v85
	v_mul_f32_e32 v46, v92, v46
	v_mul_f32_e32 v47, v93, v47
	v_mov_b32_e32 v56, v81
	v_mul_f32_e32 v84, v44, v46
	v_mul_f32_e32 v85, v44, v47
	v_mul_f32_e32 v44, -1.0, v92
	v_mul_f32_e32 v45, -1.0, v93
	v_mov_b32_e32 v46, v52
	v_mov_b32_e32 v45, v79
	v_mul_f32_e32 v44, v80, v44
	v_mul_f32_e32 v45, v81, v45
	v_mov_b32_e32 v47, v58
	v_cvt_pk_bf16_f32 v44, v44, v45
	v_cvt_pk_bf16_f32 v45, v84, v85
	ds_write_b16 v75, v44 offset:2160
	ds_write_b16_d16_hi v75, v44 offset:4464
	ds_write_b16 v74, v45 offset:2160
	ds_write_b16_d16_hi v74, v45 offset:4464
	v_mov_b32_e32 v44, v48
	v_mov_b32_e32 v45, v50
	v_mul_f32_e32 v44, v56, v44
	v_mul_f32_e32 v45, v56, v45
	v_mul_f32_e32 v46, v56, v46
	v_mul_f32_e32 v47, v56, v47
	v_mov_b32_e32 v50, v49
	v_mov_b32_e32 v58, v53
	v_cvt_pk_bf16_f32 v44, v44, v45
	v_cvt_pk_bf16_f32 v45, v46, v47
	v_mul_f32_e32 v46, v50, v56
	v_mul_f32_e32 v47, v51, v56
	v_mul_f32_e32 v48, v58, v56
	v_mul_f32_e32 v49, v59, v56
	v_cvt_pk_bf16_f32 v46, v46, v47
	v_cvt_pk_bf16_f32 v47, v48, v49
	v_add_u32_e32 v50, s89, v238
	ds_write_b128 v50, v[44:47] offset:4608
	v_mov_b32_e32 v44, v60
	v_mov_b32_e32 v45, v62
	v_mov_b32_e32 v46, v64
	v_mov_b32_e32 v47, v66
	v_mul_f32_e32 v44, v56, v44
	v_mul_f32_e32 v45, v56, v45
	v_mul_f32_e32 v46, v56, v46
	v_mul_f32_e32 v47, v56, v47
	v_mov_b32_e32 v62, v61
	v_mov_b32_e32 v66, v65
	v_cvt_pk_bf16_f32 v44, v44, v45
	v_cvt_pk_bf16_f32 v45, v46, v47
	v_mul_f32_e32 v46, v62, v56
	v_mul_f32_e32 v47, v63, v56
	v_mul_f32_e32 v48, v66, v56
	v_mul_f32_e32 v49, v67, v56
	v_cvt_pk_bf16_f32 v46, v46, v47
	v_cvt_pk_bf16_f32 v47, v48, v49
	ds_write_b128 v50, v[44:47] offset:4624
	v_mov_b32_e32 v44, v68
	v_mov_b32_e32 v45, v70
	v_mov_b32_e32 v46, v86
	v_mov_b32_e32 v47, v54
	v_mul_f32_e32 v44, v56, v44
	v_mul_f32_e32 v45, v56, v45
	v_mul_f32_e32 v46, v56, v46
	v_mul_f32_e32 v47, v56, v47
	v_mov_b32_e32 v70, v69
	v_mov_b32_e32 v54, v87
	v_cvt_pk_bf16_f32 v44, v44, v45
	v_cvt_pk_bf16_f32 v45, v46, v47
	v_mul_f32_e32 v46, v70, v56
	v_mul_f32_e32 v47, v71, v56
	v_mul_f32_e32 v48, v54, v56
	v_mul_f32_e32 v49, v55, v56
	v_cvt_pk_bf16_f32 v46, v46, v47
	v_cvt_pk_bf16_f32 v47, v48, v49
	ds_write_b128 v50, v[44:47] offset:4640
	v_mov_b32_e32 v44, v82
	v_mov_b32_e32 v45, v88
	v_mov_b32_e32 v46, v90
	v_mov_b32_e32 v47, v84
	v_mul_f32_e32 v44, v56, v44
	v_mul_f32_e32 v45, v56, v45
	v_mul_f32_e32 v46, v56, v46
	v_mul_f32_e32 v47, v56, v47
	v_mov_b32_e32 v88, v83
	v_mov_b32_e32 v84, v91
	v_cvt_pk_bf16_f32 v44, v44, v45
	v_cvt_pk_bf16_f32 v45, v46, v47
	v_mul_f32_e32 v46, v56, v88
	v_mul_f32_e32 v47, v56, v89
	v_mul_f32_e32 v48, v56, v84
	v_mul_f32_e32 v49, v56, v85
	v_cvt_pk_bf16_f32 v46, v46, v47
	v_cvt_pk_bf16_f32 v47, v48, v49
	ds_write_b128 v50, v[44:47] offset:4656
	v_add_u32_e32 v44, s89, v220
	ds_write_b32 v44, v81 offset:12800
	s_waitcnt lgkmcnt(0)
	v_add3_u32 v75, s89, v186, v191
	ds_read_b128 v[44:47], v75
	ds_read_b128 v[48:51], v211
	ds_read_b128 v[52:55], v75 offset:64
	ds_read_b128 v[56:59], v211 offset:64
	ds_read_b128 v[64:67], v211 offset:2304
	ds_read_b128 v[68:71], v211 offset:2368
	ds_read_b128 v[80:83], v75 offset:2304
	ds_read_b128 v[84:87], v75 offset:2368
	s_waitcnt lgkmcnt(6)
	v_mfma_f32_16x16x32_bf16 v[60:63], v[44:47], v[48:51], 0
	s_add_i32 s87, s87, 4
	s_cmpk_eq_i32 s85, 0x103
	s_waitcnt vmcnt(0)
	v_mov_b32_e32 v75, v78
	s_waitcnt lgkmcnt(3)
	v_mfma_f32_16x16x32_bf16 v[44:47], v[44:47], v[64:67], 0
	s_waitcnt lgkmcnt(1)
	v_mfma_f32_16x16x32_bf16 v[48:51], v[80:83], v[48:51], 0
	v_mfma_f32_16x16x32_bf16 v[64:67], v[80:83], v[64:67], 0
	v_mfma_f32_16x16x32_bf16 v[60:63], v[52:55], v[56:59], v[60:63]
	v_mfma_f32_16x16x32_bf16 v[44:47], v[52:55], v[68:71], v[44:47]
	s_waitcnt lgkmcnt(0)
	v_mfma_f32_16x16x32_bf16 v[48:51], v[84:87], v[56:59], v[48:51]
	v_add3_u32 v56, s89, v239, v240
	s_nop 3
	v_cndmask_b32_e64 v57, 0, v60, s[14:15]
	v_cndmask_b32_e64 v44, 0, v44, s[14:15]
	v_mfma_f32_16x16x32_bf16 v[52:55], v[84:87], v[68:71], v[64:67]
	v_add_u32_e32 v58, s73, v243
	v_cndmask_b32_e64 v48, v48, 0, s[16:17]
	ds_write2st64_b32 v58, v57, v44 offset1:4
	v_cndmask_b32_e64 v45, v45, 0, s[16:17]
	s_nop 3
	v_cndmask_b32_e64 v52, v52, 0, s[16:17]
	v_cvt_pk_bf16_f32 v44, v48, v52
	v_add_u32_e32 v48, v56, v242
	ds_write_b16 v48, v44 offset:9728
	ds_write_b16_d16_hi v48, v44 offset:9736
	v_cndmask_b32_e64 v44, v61, 0, s[16:17]
	v_cndmask_b32_e64 v48, v49, 0, s[18:19]
	v_cndmask_b32_e64 v49, v53, 0, s[18:19]
	v_add_u32_e32 v52, s73, v245
	ds_write2st64_b32 v52, v44, v45 offset1:4
	v_cvt_pk_bf16_f32 v44, v48, v49
	v_add_u32_e32 v45, v56, v244
	ds_write_b16 v45, v44 offset:9728
	ds_write_b16_d16_hi v45, v44 offset:9736
	v_cndmask_b32_e64 v44, 0, v62, s[20:21]
	v_cndmask_b32_e64 v45, 0, v46, s[20:21]
	v_cndmask_b32_e64 v46, v50, 0, s[22:23]
	v_cndmask_b32_e64 v48, v54, 0, s[22:23]
	v_add_u32_e32 v49, s73, v247
	ds_write2st64_b32 v49, v44, v45 offset1:4
	v_cvt_pk_bf16_f32 v44, v46, v48
	v_add_u32_e32 v45, v56, v246
	ds_write_b16 v45, v44 offset:9728
	ds_write_b16_d16_hi v45, v44 offset:9736
	v_cndmask_b32_e64 v44, 0, v63, s[24:25]
	v_cndmask_b32_e64 v45, 0, v47, s[24:25]
	v_cndmask_b32_e64 v46, v51, 0, s[26:27]
	v_cndmask_b32_e64 v47, v55, 0, s[26:27]
	v_add_u32_e32 v48, s73, v249
	ds_write2st64_b32 v48, v44, v45 offset1:4
	v_cvt_pk_bf16_f32 v44, v46, v47
	v_add_u32_e32 v45, v56, v248
	ds_write_b16 v45, v44 offset:9728
	ds_write_b16_d16_hi v45, v44 offset:9736
	s_waitcnt lgkmcnt(0)
	s_barrier
	s_cbranch_scc1 .LBB0_1719
